# speedup vs baseline: 1.0157x; 1.0014x over previous
.LBB1_136:
	v_add_u32_e32 v128, 16, v146
	v_lshlrev_b32_e32 v128, 8, v128
	v_and_b32_e32 v128, 0x7ff00, v128
	v_add_u32_e32 v128, v128, v144
	global_load_dwordx4 v[66:69], v128, s[22:23] offset:16
	global_load_dwordx4 v[134:137], v128, s[22:23]
	s_waitcnt vmcnt(0)
	v_mul_f32_e32 v126, v115, v135
	v_mul_f32_e32 v127, v115, v134
	v_fma_f32 v118, v114, v134, -v126
	v_fma_f32 v119, v114, v135, v127
	v_mul_f32_e32 v126, v117, v137
	v_mul_f32_e32 v127, v117, v136
	v_fma_f32 v120, v116, v136, -v126
	v_fma_f32 v121, v116, v137, v127
	v_mul_f32_e32 v126, v111, v67
	v_mul_f32_e32 v127, v111, v66
	v_fma_f32 v122, v110, v66, -v126
	v_fma_f32 v123, v110, v67, v127
	v_mul_f32_e32 v126, v113, v69
	v_mul_f32_e32 v127, v113, v68
	v_fma_f32 v124, v112, v68, -v126
	v_fma_f32 v125, v112, v69, v127
	v_pk_mul_f32 v[118:119], v[138:139], v[118:119]
	v_pk_mul_f32 v[120:121], v[138:139], v[120:121]
	v_pk_mul_f32 v[122:123], v[138:139], v[122:123]
	v_pk_mul_f32 v[124:125], v[138:139], v[124:125]
	v_cvt_pk_f16_f32 v188, v118, v119
	v_cvt_pk_f16_f32 v189, v120, v121
	v_cvt_pk_f16_f32 v190, v122, v123
	v_cvt_pk_f16_f32 v191, v124, v125
	v_mul_f32_e32 v126, v107, v135
	v_mul_f32_e32 v127, v107, v134
	v_fma_f32 v118, v106, v134, -v126
	v_fma_f32 v119, v106, v135, v127
	v_mul_f32_e32 v126, v109, v137
	v_mul_f32_e32 v127, v109, v136
	v_fma_f32 v120, v108, v136, -v126
	v_fma_f32 v121, v108, v137, v127
	v_mul_f32_e32 v126, v103, v67
	v_mul_f32_e32 v127, v103, v66
	v_fma_f32 v122, v102, v66, -v126
	v_fma_f32 v123, v102, v67, v127
	v_mul_f32_e32 v126, v105, v69
	v_mul_f32_e32 v127, v105, v68
	v_fma_f32 v124, v104, v68, -v126
	v_fma_f32 v125, v104, v69, v127
	v_pk_mul_f32 v[118:119], v[138:139], v[118:119]
	v_pk_mul_f32 v[120:121], v[138:139], v[120:121]
	v_pk_mul_f32 v[122:123], v[138:139], v[122:123]
	v_pk_mul_f32 v[124:125], v[138:139], v[124:125]
	v_cvt_pk_f16_f32 v192, v118, v119
	v_cvt_pk_f16_f32 v193, v120, v121
	v_cvt_pk_f16_f32 v194, v122, v123
	v_cvt_pk_f16_f32 v195, v124, v125
	v_add_u32_e32 v128, 32, v146
	v_lshlrev_b32_e32 v128, 8, v128
	v_and_b32_e32 v128, 0x7ff00, v128
	v_add_u32_e32 v128, v128, v144
	global_load_dwordx4 v[66:69], v128, s[22:23] offset:16
	global_load_dwordx4 v[134:137], v128, s[22:23]
	s_waitcnt vmcnt(0)
	v_mul_f32_e32 v126, v99, v135
	v_mul_f32_e32 v127, v99, v134
	v_fma_f32 v118, v98, v134, -v126
	v_fma_f32 v119, v98, v135, v127
	v_mul_f32_e32 v126, v101, v137
	v_mul_f32_e32 v127, v101, v136
	v_fma_f32 v120, v100, v136, -v126
	v_fma_f32 v121, v100, v137, v127
	v_mul_f32_e32 v126, v95, v67
	v_mul_f32_e32 v127, v95, v66
	v_fma_f32 v122, v94, v66, -v126
	v_fma_f32 v123, v94, v67, v127
	v_mul_f32_e32 v126, v97, v69
	v_mul_f32_e32 v127, v97, v68
	v_fma_f32 v124, v96, v68, -v126
	v_fma_f32 v125, v96, v69, v127
	v_pk_mul_f32 v[118:119], v[138:139], v[118:119]
	v_pk_mul_f32 v[120:121], v[138:139], v[120:121]
	v_pk_mul_f32 v[122:123], v[138:139], v[122:123]
	v_pk_mul_f32 v[124:125], v[138:139], v[124:125]
	v_cvt_pk_f16_f32 v196, v118, v119
	v_cvt_pk_f16_f32 v197, v120, v121
	v_cvt_pk_f16_f32 v198, v122, v123
	v_cvt_pk_f16_f32 v199, v124, v125
	v_mul_f32_e32 v126, v91, v135
	v_mul_f32_e32 v127, v91, v134
	v_fma_f32 v118, v90, v134, -v126
	v_fma_f32 v119, v90, v135, v127
	v_mul_f32_e32 v126, v93, v137
	v_mul_f32_e32 v127, v93, v136
	v_fma_f32 v120, v92, v136, -v126
	v_fma_f32 v121, v92, v137, v127
	v_mul_f32_e32 v126, v87, v67
	v_mul_f32_e32 v127, v87, v66
	v_fma_f32 v122, v86, v66, -v126
	v_fma_f32 v123, v86, v67, v127
	v_mul_f32_e32 v126, v89, v69
	v_mul_f32_e32 v127, v89, v68
	v_fma_f32 v124, v88, v68, -v126
	v_fma_f32 v125, v88, v69, v127
	v_pk_mul_f32 v[118:119], v[138:139], v[118:119]
	v_pk_mul_f32 v[120:121], v[138:139], v[120:121]
	v_pk_mul_f32 v[122:123], v[138:139], v[122:123]
	v_pk_mul_f32 v[124:125], v[138:139], v[124:125]
	v_cvt_pk_f16_f32 v200, v118, v119
	v_cvt_pk_f16_f32 v201, v120, v121
	v_cvt_pk_f16_f32 v202, v122, v123
	v_cvt_pk_f16_f32 v203, v124, v125
	v_add_u32_e32 v128, 48, v146
	v_lshlrev_b32_e32 v128, 8, v128
	v_and_b32_e32 v128, 0x7ff00, v128
	v_add_u32_e32 v128, v128, v144
	global_load_dwordx4 v[66:69], v128, s[22:23] offset:16
	global_load_dwordx4 v[134:137], v128, s[22:23]
	s_waitcnt vmcnt(0)
	v_mul_f32_e32 v126, v83, v135
	v_mul_f32_e32 v127, v83, v134
	v_fma_f32 v118, v82, v134, -v126
	v_fma_f32 v119, v82, v135, v127
	v_mul_f32_e32 v126, v85, v137
	v_mul_f32_e32 v127, v85, v136
	v_fma_f32 v120, v84, v136, -v126
	v_fma_f32 v121, v84, v137, v127
	v_mul_f32_e32 v126, v79, v67
	v_mul_f32_e32 v127, v79, v66
	v_fma_f32 v122, v78, v66, -v126
	v_fma_f32 v123, v78, v67, v127
	v_mul_f32_e32 v126, v81, v69
	v_mul_f32_e32 v127, v81, v68
	v_fma_f32 v124, v80, v68, -v126
	v_fma_f32 v125, v80, v69, v127
	v_pk_mul_f32 v[118:119], v[138:139], v[118:119]
	v_pk_mul_f32 v[120:121], v[138:139], v[120:121]
	v_pk_mul_f32 v[122:123], v[138:139], v[122:123]
	v_pk_mul_f32 v[124:125], v[138:139], v[124:125]
	v_cvt_pk_f16_f32 v204, v118, v119
	v_cvt_pk_f16_f32 v205, v120, v121
	v_cvt_pk_f16_f32 v206, v122, v123
	v_cvt_pk_f16_f32 v207, v124, v125
	v_mul_f32_e32 v126, v75, v135
	v_mul_f32_e32 v127, v75, v134
	v_fma_f32 v118, v74, v134, -v126
	v_fma_f32 v119, v74, v135, v127
	v_mul_f32_e32 v126, v77, v137
	v_mul_f32_e32 v127, v77, v136
	v_fma_f32 v120, v76, v136, -v126
	v_fma_f32 v121, v76, v137, v127
	v_mul_f32_e32 v126, v71, v67
	v_mul_f32_e32 v127, v71, v66
	v_fma_f32 v122, v70, v66, -v126
	v_fma_f32 v123, v70, v67, v127
	v_mul_f32_e32 v126, v73, v69
	v_mul_f32_e32 v127, v73, v68
	v_fma_f32 v124, v72, v68, -v126
	v_fma_f32 v125, v72, v69, v127
	v_pk_mul_f32 v[118:119], v[138:139], v[118:119]
	v_pk_mul_f32 v[120:121], v[138:139], v[120:121]
	v_pk_mul_f32 v[122:123], v[138:139], v[122:123]
	v_pk_mul_f32 v[124:125], v[138:139], v[124:125]
	v_cvt_pk_f16_f32 v208, v118, v119
	v_cvt_pk_f16_f32 v209, v120, v121
	v_cvt_pk_f16_f32 v210, v122, v123
	v_cvt_pk_f16_f32 v211, v124, v125
	v_add_u32_e32 v128, 0x80, v146
	v_lshlrev_b32_e32 v128, 8, v128
	v_and_b32_e32 v128, 0x7ff00, v128
	v_add_u32_e32 v128, v128, v144
	global_load_dwordx4 v[66:69], v128, s[22:23] offset:16
	global_load_dwordx4 v[134:137], v128, s[22:23]
	s_waitcnt vmcnt(0)
	v_mul_f32_e32 v126, v63, v135
	v_mul_f32_e32 v127, v63, v134
	v_fma_f32 v118, v62, v134, -v126
	v_fma_f32 v119, v62, v135, v127
	v_mul_f32_e32 v126, v65, v137
	v_mul_f32_e32 v127, v65, v136
	v_fma_f32 v120, v64, v136, -v126
	v_fma_f32 v121, v64, v137, v127
	v_mul_f32_e32 v126, v59, v67
	v_mul_f32_e32 v127, v59, v66
	v_fma_f32 v122, v58, v66, -v126
	v_fma_f32 v123, v58, v67, v127
	v_mul_f32_e32 v126, v61, v69
	v_mul_f32_e32 v127, v61, v68
	v_fma_f32 v124, v60, v68, -v126
	v_fma_f32 v125, v60, v69, v127
	v_pk_mul_f32 v[118:119], v[138:139], v[118:119]
	v_pk_mul_f32 v[120:121], v[138:139], v[120:121]
	v_pk_mul_f32 v[122:123], v[138:139], v[122:123]
	v_pk_mul_f32 v[124:125], v[138:139], v[124:125]
	v_cvt_pk_f16_f32 v212, v118, v119
	v_cvt_pk_f16_f32 v213, v120, v121
	v_cvt_pk_f16_f32 v214, v122, v123
	v_cvt_pk_f16_f32 v215, v124, v125
	v_mul_f32_e32 v126, v55, v135
	v_mul_f32_e32 v127, v55, v134
	v_fma_f32 v118, v54, v134, -v126
	v_fma_f32 v119, v54, v135, v127
	v_mul_f32_e32 v126, v57, v137
	v_mul_f32_e32 v127, v57, v136
	v_fma_f32 v120, v56, v136, -v126
	v_fma_f32 v121, v56, v137, v127
	v_mul_f32_e32 v126, v51, v67
	v_mul_f32_e32 v127, v51, v66
	v_fma_f32 v122, v50, v66, -v126
	v_fma_f32 v123, v50, v67, v127
	v_mul_f32_e32 v126, v53, v69
	v_mul_f32_e32 v127, v53, v68
	v_fma_f32 v124, v52, v68, -v126
	v_fma_f32 v125, v52, v69, v127
	v_pk_mul_f32 v[118:119], v[138:139], v[118:119]
	v_pk_mul_f32 v[120:121], v[138:139], v[120:121]
	v_pk_mul_f32 v[122:123], v[138:139], v[122:123]
	v_pk_mul_f32 v[124:125], v[138:139], v[124:125]
	v_cvt_pk_f16_f32 v216, v118, v119
	v_cvt_pk_f16_f32 v217, v120, v121
	v_cvt_pk_f16_f32 v218, v122, v123
	v_cvt_pk_f16_f32 v219, v124, v125
	v_add_u32_e32 v128, 0x90, v146
	v_lshlrev_b32_e32 v128, 8, v128
	v_and_b32_e32 v128, 0x7ff00, v128
	v_add_u32_e32 v128, v128, v144
	global_load_dwordx4 v[66:69], v128, s[22:23] offset:16
	global_load_dwordx4 v[134:137], v128, s[22:23]
	s_waitcnt vmcnt(0)
	v_mul_f32_e32 v126, v47, v135
	v_mul_f32_e32 v127, v47, v134
	v_fma_f32 v118, v46, v134, -v126
	v_fma_f32 v119, v46, v135, v127
	v_mul_f32_e32 v126, v49, v137
	v_mul_f32_e32 v127, v49, v136
	v_fma_f32 v120, v48, v136, -v126
	v_fma_f32 v121, v48, v137, v127
	v_mul_f32_e32 v126, v43, v67
	v_mul_f32_e32 v127, v43, v66
	v_fma_f32 v122, v42, v66, -v126
	v_fma_f32 v123, v42, v67, v127
	v_mul_f32_e32 v126, v45, v69
	v_mul_f32_e32 v127, v45, v68
	v_fma_f32 v124, v44, v68, -v126
	v_fma_f32 v125, v44, v69, v127
	v_pk_mul_f32 v[118:119], v[138:139], v[118:119]
	v_pk_mul_f32 v[120:121], v[138:139], v[120:121]
	v_pk_mul_f32 v[122:123], v[138:139], v[122:123]
	v_pk_mul_f32 v[124:125], v[138:139], v[124:125]
	v_cvt_pk_f16_f32 v220, v118, v119
	v_cvt_pk_f16_f32 v221, v120, v121
	v_cvt_pk_f16_f32 v222, v122, v123
	v_cvt_pk_f16_f32 v223, v124, v125
	v_mul_f32_e32 v126, v39, v135
	v_mul_f32_e32 v127, v39, v134
	v_fma_f32 v118, v38, v134, -v126
	v_fma_f32 v119, v38, v135, v127
	v_mul_f32_e32 v126, v41, v137
	v_mul_f32_e32 v127, v41, v136
	v_fma_f32 v120, v40, v136, -v126
	v_fma_f32 v121, v40, v137, v127
	v_mul_f32_e32 v126, v35, v67
	v_mul_f32_e32 v127, v35, v66
	v_fma_f32 v122, v34, v66, -v126
	v_fma_f32 v123, v34, v67, v127
	v_mul_f32_e32 v126, v37, v69
	v_mul_f32_e32 v127, v37, v68
	v_fma_f32 v124, v36, v68, -v126
	v_fma_f32 v125, v36, v69, v127
	v_pk_mul_f32 v[118:119], v[138:139], v[118:119]
	v_pk_mul_f32 v[120:121], v[138:139], v[120:121]
	v_pk_mul_f32 v[122:123], v[138:139], v[122:123]
	v_pk_mul_f32 v[124:125], v[138:139], v[124:125]
	v_cvt_pk_f16_f32 v224, v118, v119
	v_cvt_pk_f16_f32 v225, v120, v121
	v_cvt_pk_f16_f32 v226, v122, v123
	v_cvt_pk_f16_f32 v227, v124, v125
	v_add_u32_e32 v128, 0xa0, v146
	v_lshlrev_b32_e32 v128, 8, v128
	v_and_b32_e32 v128, 0x7ff00, v128
	v_add_u32_e32 v128, v128, v144
	global_load_dwordx4 v[66:69], v128, s[22:23] offset:16
	global_load_dwordx4 v[134:137], v128, s[22:23]
	s_waitcnt vmcnt(0)
	v_mul_f32_e32 v126, v31, v135
	v_mul_f32_e32 v127, v31, v134
	v_fma_f32 v118, v30, v134, -v126
	v_fma_f32 v119, v30, v135, v127
	v_mul_f32_e32 v126, v33, v137
	v_mul_f32_e32 v127, v33, v136
	v_fma_f32 v120, v32, v136, -v126
	v_fma_f32 v121, v32, v137, v127
	v_mul_f32_e32 v126, v27, v67
	v_mul_f32_e32 v127, v27, v66
	v_fma_f32 v122, v26, v66, -v126
	v_fma_f32 v123, v26, v67, v127
	v_mul_f32_e32 v126, v29, v69
	v_mul_f32_e32 v127, v29, v68
	v_fma_f32 v124, v28, v68, -v126
	v_fma_f32 v125, v28, v69, v127
	v_pk_mul_f32 v[118:119], v[138:139], v[118:119]
	v_pk_mul_f32 v[120:121], v[138:139], v[120:121]
	v_pk_mul_f32 v[122:123], v[138:139], v[122:123]
	v_pk_mul_f32 v[124:125], v[138:139], v[124:125]
	v_cvt_pk_f16_f32 v228, v118, v119
	v_cvt_pk_f16_f32 v229, v120, v121
	v_cvt_pk_f16_f32 v230, v122, v123
	v_cvt_pk_f16_f32 v231, v124, v125
	v_mul_f32_e32 v126, v23, v135
	v_mul_f32_e32 v127, v23, v134
	v_fma_f32 v118, v22, v134, -v126
	v_fma_f32 v119, v22, v135, v127
	v_mul_f32_e32 v126, v25, v137
	v_mul_f32_e32 v127, v25, v136
	v_fma_f32 v120, v24, v136, -v126
	v_fma_f32 v121, v24, v137, v127
	v_mul_f32_e32 v126, v19, v67
	v_mul_f32_e32 v127, v19, v66
	v_fma_f32 v122, v18, v66, -v126
	v_fma_f32 v123, v18, v67, v127
	v_mul_f32_e32 v126, v21, v69
	v_mul_f32_e32 v127, v21, v68
	v_fma_f32 v124, v20, v68, -v126
	v_fma_f32 v125, v20, v69, v127
	v_pk_mul_f32 v[118:119], v[138:139], v[118:119]
	v_pk_mul_f32 v[120:121], v[138:139], v[120:121]
	v_pk_mul_f32 v[122:123], v[138:139], v[122:123]
	v_pk_mul_f32 v[124:125], v[138:139], v[124:125]
	v_cvt_pk_f16_f32 v232, v118, v119
	v_cvt_pk_f16_f32 v233, v120, v121
	v_cvt_pk_f16_f32 v234, v122, v123
	v_cvt_pk_f16_f32 v235, v124, v125
	v_add_u32_e32 v128, 0xb0, v146
	v_lshlrev_b32_e32 v128, 8, v128
	v_and_b32_e32 v128, 0x7ff00, v128
	v_add_u32_e32 v128, v128, v144
	global_load_dwordx4 v[66:69], v128, s[22:23] offset:16
	global_load_dwordx4 v[134:137], v128, s[22:23]
	s_waitcnt vmcnt(0)
	v_mul_f32_e32 v126, v15, v135
	v_mul_f32_e32 v127, v15, v134
	v_fma_f32 v118, v14, v134, -v126
	v_fma_f32 v119, v14, v135, v127
	v_mul_f32_e32 v126, v17, v137
	v_mul_f32_e32 v127, v17, v136
	v_fma_f32 v120, v16, v136, -v126
	v_fma_f32 v121, v16, v137, v127
	v_mul_f32_e32 v126, v11, v67
	v_mul_f32_e32 v127, v11, v66
	v_fma_f32 v122, v10, v66, -v126
	v_fma_f32 v123, v10, v67, v127
	v_mul_f32_e32 v126, v13, v69
	v_mul_f32_e32 v127, v13, v68
	v_fma_f32 v124, v12, v68, -v126
	v_fma_f32 v125, v12, v69, v127
	v_pk_mul_f32 v[118:119], v[138:139], v[118:119]
	v_pk_mul_f32 v[120:121], v[138:139], v[120:121]
	v_pk_mul_f32 v[122:123], v[138:139], v[122:123]
	v_pk_mul_f32 v[124:125], v[138:139], v[124:125]
	v_cvt_pk_f16_f32 v236, v118, v119
	v_cvt_pk_f16_f32 v237, v120, v121
	v_cvt_pk_f16_f32 v238, v122, v123
	v_cvt_pk_f16_f32 v239, v124, v125
	v_mul_f32_e32 v126, v7, v135
	v_mul_f32_e32 v127, v7, v134
	v_fma_f32 v118, v6, v134, -v126
	v_fma_f32 v119, v6, v135, v127
	v_mul_f32_e32 v126, v9, v137
	v_mul_f32_e32 v127, v9, v136
	v_fma_f32 v120, v8, v136, -v126
	v_fma_f32 v121, v8, v137, v127
	v_mul_f32_e32 v126, v3, v67
	v_mul_f32_e32 v127, v3, v66
	v_fma_f32 v122, v2, v66, -v126
	v_fma_f32 v123, v2, v67, v127
	v_mul_f32_e32 v126, v5, v69
	v_mul_f32_e32 v127, v5, v68
	v_fma_f32 v124, v4, v68, -v126
	v_fma_f32 v125, v4, v69, v127
	v_pk_mul_f32 v[118:119], v[138:139], v[118:119]
	v_pk_mul_f32 v[120:121], v[138:139], v[120:121]
	v_pk_mul_f32 v[122:123], v[138:139], v[122:123]
	v_pk_mul_f32 v[124:125], v[138:139], v[124:125]
	v_cvt_pk_f16_f32 v160, v118, v119
	v_cvt_pk_f16_f32 v161, v120, v121
	v_cvt_pk_f16_f32 v162, v122, v123
	v_cvt_pk_f16_f32 v163, v124, v125
